# combo4: adds light-tile K-loop DMA trimming (A rows >=128 never read by light tiles; rows 64..127 skipped when the tile has <=64 rows)
# speedup vs baseline: 1.0113x; 1.0113x over previous
; __device__ __forceinline__ int tid_opaque() { int t = threadIdx.x; asm volatile("" : "+v"(t)); return t; }
; __device__ __forceinline__ __amdgpu_buffer_rsrc_t mk_rsrc(const void* p) { return __builtin_amdgcn_make_buffer_rsrc((void*)p, 0, 0x7ffffff0, 0x00020000); }
;     __device__ __forceinline__ void init() {
;         const int tid = tid_opaque(), wid = tid >> 6, lane = tid & 63;
;         wr = wid >> 2; wc = wid & 3; fr = lane & 15; fq = lane >> 4;
;         aR = (wid >> 1) * 16 + (lane >> 2); aC = (wid & 1) * 32 + (((lane & 3) ^ ((lane >> 5) << 1)) * 8);
;         a_w = (unsigned)(wid * 1024 + lane * 16);
;         { const int l32 = lane & 31, kc8 = 2 * (wid >> 1) + (lane >> 5), wc_ = l32 >> 3, bfq = (l32 >> 1) & 3, nlo = l32 & 1; b_p = wid & 1;
;           b_k = kc8 * 8; b_col = wc_ * 64 + b_p * 32 + bfq * 8 + nlo * 4; b_gucol = wc_ * 32 + bfq * 8 + nlo * 4;
;           const int sub = wc_ * 4 + 2 * b_p + nlo;
;           b_w = (unsigned)((sub * 2 + (kc8 >> 2)) * 1024 + (((4 * bfq) * 64 + (kc8 & 3) * 16) ^ ((bfq >> 1) << 5))); b_rot = (unsigned)(nlo * 64); }
;         const unsigned lo = (unsigned)((fr * 64 + fq * 16) ^ ((fr >> 3) << 5));
;         a_r = (unsigned)(wr * 16384) + lo; b_r = 32768u + (unsigned)(wc * 8192) + lo;
; __device__ __forceinline__ void phase_moe_gu(const Ptrs& p, LAS unsigned char* lds) {
;     ...
;         const int* list = (const int*)(p.ws + OFF_LIST) + (size_t)mu.e * NTOK; const int i0 = mu.mt * 256, n0 = mu.nt * 128;
;         unsigned ao[4];
; #pragma unroll
;         for (int i = 0; i < 4; ++i) { const int r = i0 + T.aR + 64 * i; const int tok = (r < mu.cnt) ? (list[r] >> 2) : 0; ao[i] = (unsigned)((tok * D + T.aC) * 2); }
;         const float* wsel = ((__builtin_amdgcn_readfirstlane(T.b_p) & 1) ? p.w_up : p.w_gate) + (size_t)mu.e * D * D + n0;
;         const unsigned bo = (unsigned)((T.b_k * D + T.b_gucol) * 4);
;         f32x4 acc[8][4]; acc_zero(acc);
;         const int mlim = __builtin_amdgcn_readfirstlane(T.wr) ? 0 : ((mu.cnt - i0 + 15) >> 4);
;         if (mu.light) gemm_kloop_light(acc, lds, T, mk_rsrc(h2), ao[0], ao[1], ao[2], ao[3], mk_rsrc(wsel), bo, D * 4u, D / 64, mlim);
.LBB0_1163:
	s_andn2_b64 vcc, exec, s[0:1]
	s_mov_b64 s[0:1], -1
	s_cbranch_vccnz .LBB0_1005
	s_ashr_i32 s43, s42, 31
	s_lshl_b64 s[0:1], s[42:43], 15
	v_mov_b32_e32 v3, v0
	s_add_u32 s0, s52, s0
	s_addc_u32 s1, s53, s1
	v_bfe_u32 v4, v3, 2, 4
	s_lshl_b32 s2, s86, 8
	v_ashrrev_i32_e32 v10, 7, v3
	v_or_b32_e32 v4, s2, v4
	v_lshl_add_u32 v4, v10, 4, v4
	v_cmp_gt_i32_e32 vcc, s87, v4
	v_mov_b32_e32 v6, 0
	v_ashrrev_i32_e32 v5, 31, v4
	v_mov_b32_e32 v7, 0
	v_mov_b32_e32 v8, 0
	v_mov_b32_e32 v9, 0
	v_lshl_add_u64 v[12:13], v[4:5], 2, s[0:1]
	s_and_saveexec_b64 s[4:5], vcc
	global_load_dword v7, v[12:13], off
	s_or_b64 exec, exec, s[4:5]
	v_add_u32_e32 v11, 64, v4
	v_cmp_gt_i32_e32 vcc, s87, v11
	s_and_saveexec_b64 s[4:5], vcc
	global_load_dword v6, v[12:13], off offset:256
	s_or_b64 exec, exec, s[4:5]
	v_add_u32_e32 v11, 0x80, v4
	v_cmp_gt_i32_e32 vcc, s87, v11
	s_and_saveexec_b64 s[4:5], vcc
	global_load_dword v9, v[12:13], off offset:512
	s_or_b64 exec, exec, s[4:5]
	v_add_u32_e32 v11, 0xc0, v4
	v_cmp_gt_i32_e32 vcc, s87, v11
	s_and_saveexec_b64 s[4:5], vcc
	global_load_dword v8, v[12:13], off offset:768
	s_or_b64 exec, exec, s[4:5]
	v_ashrrev_i32_e32 v5, 6, v3
	v_and_b32_e32 v11, 1, v5
	s_lshl_b32 s0, s85, 7
	v_readfirstlane_b32 s1, v11
	v_readlane_b32 s4, v246, 0
	s_bitcmp0_b32 s1, 0
	v_readlane_b32 s5, v246, 1
	s_cselect_b32 s1, s49, s5
	s_cselect_b32 s3, s48, s4
	s_lshl_b64 s[4:5], s[42:43], 24
	v_readlane_b32 s6, v246, 2
	s_add_u32 s3, s3, s4
	v_and_b32_e32 v4, 63, v3
	s_addc_u32 s6, s1, s5
	s_ashr_i32 s1, s0, 31
	v_lshrrev_b32_e32 v12, 5, v4
	v_bfe_u32 v13, v3, 1, 2
	s_lshl_b64 s[4:5], s[0:1], 2
	v_lshl_or_b32 v10, v10, 1, v12
	v_bfe_u32 v12, v3, 3, 2
	v_and_b32_e32 v14, 1, v3
	v_lshlrev_b32_e32 v15, 5, v13
	s_add_u32 s24, s3, s4
	v_lshl_or_b32 v15, v12, 7, v15
	v_lshlrev_b32_e32 v16, 16, v10
	v_lshlrev_b32_e32 v17, 4, v14
	s_addc_u32 s1, s6, s5
	v_or3_b32 v225, v15, v17, v16
	s_and_b32 s25, s1, 0xffff
	s_movk_i32 s1, 0x2000
	buffer_load_dwordx4 v[114:117], v225, s[24:27], 0 offen
	buffer_load_dwordx4 v[118:121], v225, s[24:27], s66 offen
	s_mov_b32 s3, 0x8000
	buffer_load_dwordx4 v[126:129], v225, s[24:27], s1 offen
	buffer_load_dwordx4 v[122:125], v225, s[24:27], s3 offen
	s_movk_i32 s1, 0x4000
	s_mov_b32 s3, 0xa000
	buffer_load_dwordx4 v[130:133], v225, s[24:27], s1 offen
	buffer_load_dwordx4 v[134:137], v225, s[24:27], s3 offen
	s_mov_b32 s1, 0xc000
	s_mov_b32 s3, 0xe000
	buffer_load_dwordx4 v[142:145], v225, s[24:27], s1 offen
	buffer_load_dwordx4 v[146:149], v225, s[24:27], s3 offen
	s_waitcnt vmcnt(8)
	v_lshlrev_b32_e32 v7, 10, v7
	v_and_b32_e32 v7, 0xfffff000, v7
	v_lshlrev_b32_e32 v6, 10, v6
	v_and_b32_e32 v6, 0xfffff000, v6
	v_lshlrev_b32_e32 v9, 10, v9
	v_and_b32_e32 v9, 0xfffff000, v9
	v_lshlrev_b32_e32 v8, 10, v8
	v_and_b32_e32 v8, 0xfffff000, v8
	v_lshlrev_b32_e32 v17, 4, v3
	v_lshlrev_b32_e32 v15, 6, v11
	v_and_b32_e32 v16, 32, v3
	v_and_b32_e32 v17, 48, v17
	v_bitop3_b32 v15, v17, v15, v16 bitop3:0xde
	v_or_b32_e32 v221, v9, v15
	v_lshlrev_b32_e32 v9, 2, v12
	v_lshlrev_b32_e32 v11, 1, v11
	v_or3_b32 v9, v9, v11, v14
	v_lshlrev_b32_e32 v11, 2, v3
	v_and_b32_e32 v12, 0xfffffc00, v11
	v_lshl_add_u32 v9, v9, 11, v12
	v_lshlrev_b32_e32 v12, 8, v13
	v_lshlrev_b32_e32 v10, 4, v10
	v_and_or_b32 v10, v10, 48, v12
	v_lshlrev_b32_e32 v12, 3, v3
	v_or_b32_e32 v223, v7, v15
	v_and_b32_e32 v7, 15, v3
	v_and_b32_e32 v12, 32, v12
	v_or_b32_e32 v222, v6, v15
	v_ashrrev_i32_e32 v6, 8, v3
	v_bitop3_b32 v219, v9, v10, v12 bitop3:0xf6
	v_lshlrev_b32_e32 v7, 6, v7
	v_and_b32_e32 v3, 48, v3
	v_and_b32_e32 v10, 32, v11
	v_or_b32_e32 v9, v7, v3
	v_bitop3_b32 v3, v7, v10, v3 bitop3:0x36
	v_lshlrev_b32_e32 v11, 13, v5
	v_lshlrev_b32_e32 v220, 6, v14
	v_lshlrev_b32_e32 v4, 4, v4
	v_lshlrev_b32_e32 v7, 14, v6
	v_and_or_b32 v226, v11, s66, v3
	v_cmp_eq_u32_e32 vcc, 0, v215
	v_add_u32_e32 v227, 0, v219
	v_add_u32_e32 v3, 0xc0, v220
	v_or_b32_e32 v224, v8, v15
	v_lshl_or_b32 v229, v5, 10, v4
	v_bitop3_b32 v216, v9, v7, v10 bitop3:0xde
	v_or_b32_e32 v217, 0x8000, v226
	v_readfirstlane_b32 s1, v6
	s_and_b64 vcc, exec, vcc
	v_add_u32_e32 v228, v227, v220
	v_and_b32_e32 v218, 0xc0, v3
	v_readlane_b32 s7, v246, 3
	v_readlane_b32 s8, v246, 4
	v_readlane_b32 s9, v246, 5
	v_readlane_b32 s10, v246, 6
	v_readlane_b32 s11, v246, 7
	s_cbranch_vccnz .LBB0_1263
; #define G_DMA_A(buf, t, i_) __builtin_amdgcn_raw_ptr_buffer_load_lds(ra, (LAS void*)(lds + (buf) * 65536 + a_wu + (i_) * 8192), 16, ao##i_, (unsigned)(t) * 128u, 0, 0)
; #define G_ISSUE_B(t) do { const unsigned so_ = (unsigned)(t) * 64u * ldbB; _Pragma("unroll") for (int i_ = 0; i_ < 8; ++i_) sb[i_] = __builtin_bit_cast(f32x4, __builtin_amdgcn_raw_buffer_load_b128(rb, bo, so_ + (unsigned)i_ * ldbB, 0)); } while (0)
; #define G_RETIRE() asm volatile("s_waitcnt vmcnt(0)" : "+v"(sb[0]), "+v"(sb[1]), "+v"(sb[2]), "+v"(sb[3]), "+v"(sb[4]), "+v"(sb[5]), "+v"(sb[6]), "+v"(sb[7]) :: "memory")
; #define G_WRITE_B(buf) do { LAS unsigned char* d_ = lds + (buf) * 65536; \
;         _Pragma("unroll") for (int j_ = 0; j_ < 4; ++j_) { u32x4 w_; w_.x = cvtpk(sb[0][j_], sb[1][j_]); w_.y = cvtpk(sb[2][j_], sb[3][j_]); w_.z = cvtpk(sb[4][j_], sb[5][j_]); w_.w = cvtpk(sb[6][j_], sb[7][j_]); \
;             *(LAS u32x4*)(d_ + 32768 + T.b_w + ((T.b_rot + 64u * j_) & 255u)) = w_; } } while (0)
; #define G_BAR() do { asm volatile("s_waitcnt lgkmcnt(0)" ::: "memory"); __builtin_amdgcn_s_barrier(); asm volatile("" ::: "memory"); } while (0)
; #define G_DMA_A(buf, t, i_) __builtin_amdgcn_raw_ptr_buffer_load_lds(ra, (LAS void*)(lds + (buf) * 65536 + a_wu + (i_) * 8192), 16, ao##i_, (unsigned)(t) * 128u, 0, 0)
; #define G_ISSUE_B(t) do { const unsigned so_ = (unsigned)(t) * 64u * ldbB; _Pragma("unroll") for (int i_ = 0; i_ < 8; ++i_) sb[i_] = __builtin_bit_cast(f32x4, __builtin_amdgcn_raw_buffer_load_b128(rb, bo, so_ + (unsigned)i_ * ldbB, 0)); } while (0)
; #define G_RETIRE() asm volatile("s_waitcnt vmcnt(0)" : "+v"(sb[0]), "+v"(sb[1]), "+v"(sb[2]), "+v"(sb[3]), "+v"(sb[4]), "+v"(sb[5]), "+v"(sb[6]), "+v"(sb[7]) :: "memory")
; __device__ __forceinline__ void gemm_kloop_light(f32x4 (&acc)[8][4], LAS unsigned char* lds, const GemmT& T, ...
;     ...
;     G_ISSUE_B(0); G_DMA_A(0, 0, 0); G_DMA_A(0, 0, 1); G_DMA_A(0, 0, 2); G_DMA_A(0, 0, 3); G_RETIRE(); G_WRITE_B(0);
;     if (nt > 1) G_ISSUE_B(1);
;     G_BAR();
; __device__ __forceinline__ void phase_moe_gu(const Ptrs& p, LAS unsigned char* lds) {
;     ...
;         const int mlim = __builtin_amdgcn_readfirstlane(T.wr) ? 0 : ((mu.cnt - i0 + 15) >> 4);
	s_sub_i32 s3, s87, s2
	s_mov_b32 s99, s3
	s_add_i32 s3, s3, 15
	s_ashr_i32 s3, s3, 4
	s_cmp_eq_u32 s1, 0
	s_cselect_b32 s1, s3, 0
	v_readfirstlane_b32 s3, v229
	s_and_b32 s3, s3, 0xfffffc00
	s_add_i32 s3, s3, 0
	s_mov_b32 s38, s26
	s_mov_b32 s39, s27
	s_mov_b32 m0, s3
	s_waitcnt vmcnt(6)
	v_mov_b64_e32 v[4:5], v[118:119]
	buffer_load_dwordx4 v223, s[36:39], 0 offen lds
	s_add_i32 m0, s3, 0x2000
	s_waitcnt vmcnt(3)
	v_mov_b64_e32 v[8:9], v[134:135]
	buffer_load_dwordx4 v222, s[36:39], 0 offen lds
	s_add_i32 m0, s3, 0x4000
	v_mov_b64_e32 v[12:13], v[114:115]
	buffer_load_dwordx4 v221, s[36:39], 0 offen lds
	s_add_i32 m0, s3, 0x6000
	s_waitcnt vmcnt(3)
	v_mov_b64_e32 v[16:17], v[146:147]
	v_mov_b64_e32 v[20:21], v[130:131]
	v_mov_b64_e32 v[24:25], v[122:123]
	v_mov_b64_e32 v[28:29], v[142:143]
	v_mov_b64_e32 v[32:33], v[126:127]
	buffer_load_dwordx4 v224, s[36:39], 0 offen lds
	v_mov_b64_e32 v[6:7], v[120:121]
	v_mov_b64_e32 v[10:11], v[136:137]
	v_mov_b64_e32 v[14:15], v[116:117]
	v_mov_b64_e32 v[18:19], v[148:149]
	v_mov_b64_e32 v[22:23], v[132:133]
	v_mov_b64_e32 v[26:27], v[124:125]
	v_mov_b64_e32 v[30:31], v[144:145]
	v_mov_b64_e32 v[34:35], v[128:129]
	s_waitcnt vmcnt(0)
	buffer_load_dwordx4 v[162:165], v225, s[24:27], s67 offen
	buffer_load_dwordx4 v[166:169], v225, s[24:27], s76 offen
	buffer_load_dwordx4 v[170:173], v225, s[24:27], s77 offen
	buffer_load_dwordx4 v[174:177], v225, s[24:27], s78 offen
	buffer_load_dwordx4 v[178:181], v225, s[24:27], s79 offen
	buffer_load_dwordx4 v[182:185], v225, s[24:27], s80 offen
	buffer_load_dwordx4 v[186:189], v225, s[24:27], s81 offen
	buffer_load_dwordx4 v[190:193], v225, s[24:27], s82 offen
	s_cmp_gt_i32 s1, 0
	s_cselect_b64 s[62:63], -1, 0
	s_cmp_lg_u32 s1, 1
	v_cvt_pk_bf16_f32 v36, v12, v32
	v_cvt_pk_bf16_f32 v37, v20, v4
	v_cvt_pk_bf16_f32 v38, v24, v8
	v_cvt_pk_bf16_f32 v39, v28, v16
	s_cselect_b64 s[60:61], -1, 0
	s_cmp_gt_i32 s1, 2
	ds_write_b128 v228, v[36:39] offset:32768
	v_cvt_pk_bf16_f32 v36, v13, v33
	v_cvt_pk_bf16_f32 v37, v21, v5
	v_cvt_pk_bf16_f32 v38, v25, v9
	v_cvt_pk_bf16_f32 v39, v29, v17
	s_cselect_b64 s[58:59], -1, 0
	s_cmp_gt_i32 s1, 3
	ds_write_b128 v228, v[36:39] offset:32832
	v_cvt_pk_bf16_f32 v36, v14, v34
	v_cvt_pk_bf16_f32 v37, v22, v6
	v_cvt_pk_bf16_f32 v38, v26, v10
	v_cvt_pk_bf16_f32 v39, v30, v18
	v_cvt_pk_bf16_f32 v4, v15, v35
	v_cvt_pk_bf16_f32 v5, v23, v7
	v_cvt_pk_bf16_f32 v6, v27, v11
	v_cvt_pk_bf16_f32 v7, v31, v19
	v_add_u32_e32 v3, v227, v218
	s_cselect_b64 s[54:55], -1, 0
	s_cmp_gt_i32 s1, 4
	ds_write_b128 v228, v[36:39] offset:32896
	ds_write_b128 v3, v[4:7] offset:32768
	s_cselect_b64 s[46:47], -1, 0
	s_cmp_gt_i32 s1, 5
	s_waitcnt lgkmcnt(0)
	s_barrier
	s_cselect_b64 s[44:45], -1, 0
	s_cmp_gt_i32 s1, 6
	v_mov_b32_e32 v4, v2
	v_mov_b32_e32 v5, v2
	s_cselect_b64 s[34:35], -1, 0
	s_cmp_gt_i32 s1, 7
	v_mov_b32_e32 v3, v2
	v_mov_b64_e32 v[16:17], v[4:5]
	v_mov_b64_e32 v[8:9], v[4:5]
	v_mov_b64_e32 v[20:21], v[4:5]
	v_mov_b64_e32 v[12:13], v[4:5]
	v_mov_b64_e32 v[32:33], v[4:5]
	v_mov_b64_e32 v[24:25], v[4:5]
	v_mov_b64_e32 v[36:37], v[4:5]
	v_mov_b64_e32 v[28:29], v[4:5]
	v_mov_b64_e32 v[48:49], v[4:5]
	v_mov_b64_e32 v[40:41], v[4:5]
	v_mov_b64_e32 v[52:53], v[4:5]
	v_mov_b64_e32 v[44:45], v[4:5]
	v_mov_b64_e32 v[64:65], v[4:5]
	v_mov_b64_e32 v[56:57], v[4:5]
	v_mov_b64_e32 v[68:69], v[4:5]
	v_mov_b64_e32 v[60:61], v[4:5]
	v_mov_b64_e32 v[80:81], v[4:5]
	v_mov_b64_e32 v[72:73], v[4:5]
	v_mov_b64_e32 v[84:85], v[4:5]
	v_mov_b64_e32 v[76:77], v[4:5]
	v_mov_b64_e32 v[96:97], v[4:5]
	v_mov_b64_e32 v[88:89], v[4:5]
	v_mov_b64_e32 v[100:101], v[4:5]
	v_mov_b64_e32 v[92:93], v[4:5]
	v_mov_b64_e32 v[112:113], v[4:5]
	v_mov_b64_e32 v[104:105], v[4:5]
	v_mov_b64_e32 v[140:141], v[4:5]
	v_mov_b64_e32 v[108:109], v[4:5]
	v_mov_b64_e32 v[160:161], v[4:5]
	v_mov_b64_e32 v[152:153], v[4:5]
	v_mov_b64_e32 v[196:197], v[4:5]
	v_mov_b64_e32 v[156:157], v[4:5]
	s_mov_b32 s68, 0
	s_cselect_b64 s[22:23], -1, 0
	s_mov_b32 s69, 0x10e000
	s_movk_i32 s70, 0x80
	v_mov_b64_e32 v[14:15], v[2:3]
	v_mov_b64_e32 v[6:7], v[2:3]
	v_mov_b64_e32 v[18:19], v[2:3]
	v_mov_b64_e32 v[10:11], v[2:3]
	v_mov_b64_e32 v[30:31], v[2:3]
	v_mov_b64_e32 v[22:23], v[2:3]
	v_mov_b64_e32 v[34:35], v[2:3]
	v_mov_b64_e32 v[26:27], v[2:3]
	v_mov_b64_e32 v[46:47], v[2:3]
	v_mov_b64_e32 v[38:39], v[2:3]
	v_mov_b64_e32 v[50:51], v[2:3]
	v_mov_b64_e32 v[42:43], v[2:3]
	v_mov_b64_e32 v[62:63], v[2:3]
	v_mov_b64_e32 v[54:55], v[2:3]
	v_mov_b64_e32 v[66:67], v[2:3]
	v_mov_b64_e32 v[58:59], v[2:3]
	v_mov_b64_e32 v[78:79], v[2:3]
	v_mov_b64_e32 v[70:71], v[2:3]
	v_mov_b64_e32 v[82:83], v[2:3]
	v_mov_b64_e32 v[74:75], v[2:3]
	v_mov_b64_e32 v[94:95], v[2:3]
	v_mov_b64_e32 v[86:87], v[2:3]
	v_mov_b64_e32 v[98:99], v[2:3]
	v_mov_b64_e32 v[90:91], v[2:3]
	v_mov_b64_e32 v[110:111], v[2:3]
	v_mov_b64_e32 v[102:103], v[2:3]
	v_mov_b64_e32 v[138:139], v[2:3]
	v_mov_b64_e32 v[106:107], v[2:3]
	v_mov_b64_e32 v[158:159], v[2:3]
	v_mov_b64_e32 v[150:151], v[2:3]
	v_mov_b64_e32 v[194:195], v[2:3]
	v_mov_b64_e32 v[154:155], v[2:3]
	s_branch .LBB0_1175

; #define LAS __attribute__((address_space(3)))
; #define G_DMA_A(buf, t, i_) __builtin_amdgcn_raw_ptr_buffer_load_lds(ra, (LAS void*)(lds + (buf) * 65536 + a_wu + (i_) * 8192), 16, ao##i_, (unsigned)(t) * 128u, 0, 0)
; #define G_DMA_A(buf, t, i_) __builtin_amdgcn_raw_ptr_buffer_load_lds(ra, (LAS void*)(lds + (buf) * 65536 + a_wu + (i_) * 8192), 16, ao##i_, (unsigned)(t) * 128u, 0, 0)
; __device__ __forceinline__ void gemm_kloop_light(f32x4 (&acc)[8][4], LAS unsigned char* lds, const GemmT& T, ...
;     ...
;     for (int t = 0; t < nt; ++t) { const int cur = t & 1; const bool w1 = t + 1 < nt, i2 = t + 2 < nt;
;         if (w1) { G_DMA_A(cur ^ 1, t + 1, 0); G_DMA_A(cur ^ 1, t + 1, 1); G_DMA_A(cur ^ 1, t + 1, 2); G_DMA_A(cur ^ 1, t + 1, 3); }
;         if (mlim > 0) {
; #pragma unroll
;             for (int ks = 0; ks < 2; ++ks) { const LAS unsigned char* s_ = lds + cur * 65536 + ks * 1024; bf16x8 Bf_[4];
; #pragma unroll
;                 for (int n_ = 0; n_ < 4; ++n_) Bf_[n_] = *(const LAS bf16x8*)(s_ + T.b_r + n_ * 2048);
; #pragma unroll
;                 for (int m_ = 0; m_ < 8; ++m_) if (m_ < mlim) { const bf16x8 At_ = *(const LAS bf16x8*)(s_ + T.a_r + m_ * 2048);
; #pragma unroll
;                     for (int n_ = 0; n_ < 4; ++n_) acc[m_][n_] = __builtin_amdgcn_mfma_f32_16x16x32_bf16(Bf_[n_], At_, acc[m_][n_], 0, 0, 0); } } }
.LBB0_1175:
	s_and_b32 s6, s68, 0x10000
	s_xor_b32 s71, s6, 0x10000
	s_add_i32 s4, s3, s71
	s_mov_b32 m0, s4
	s_add_i32 s5, s4, 0x6000
	s_add_i32 s7, s4, 0x4000
	s_addk_i32 s4, 0x2000
	buffer_load_dwordx4 v223, s[36:39], s70 offen lds
	s_mov_b32 m0, s4
	v_cndmask_b32_e64 v3, 0, 1, s[62:63]
	s_cmp_lt_i32 s99, 65
	s_cbranch_scc1 .Lmy_lsk0
	buffer_load_dwordx4 v222, s[36:39], s70 offen lds
.Lmy_lsk0:
	s_mov_b32 m0, s7
	s_andn2_b64 vcc, exec, s[62:63]
	s_mov_b32 m0, s5
	v_cmp_ne_u32_e64 s[4:5], 1, v3
	s_cbranch_vccnz .LBB0_1174
	s_add_i32 s6, s6, 0
	v_add_u32_e32 v4, s6, v226
	ds_read_b128 v[198:201], v4 offset:32768
	v_add_u32_e32 v3, s6, v216
	ds_read_b128 v[202:205], v4 offset:34816
	ds_read_b128 v[230:233], v3
	ds_read_b128 v[206:209], v4 offset:36864
	ds_read_b128 v[210:213], v4 offset:38912
	s_waitcnt lgkmcnt(2)
	v_mfma_f32_16x16x32_bf16 v[194:197], v[202:205], v[230:233], v[194:197]
	v_cndmask_b32_e64 v5, 0, 1, s[60:61]
	v_cmp_ne_u32_e64 s[6:7], 1, v5
	s_andn2_b64 vcc, exec, s[60:61]
	v_mfma_f32_16x16x32_bf16 v[154:157], v[198:201], v[230:233], v[154:157]
	s_waitcnt lgkmcnt(1)
	v_mfma_f32_16x16x32_bf16 v[150:153], v[206:209], v[230:233], v[150:153]
	s_waitcnt lgkmcnt(0)
	v_mfma_f32_16x16x32_bf16 v[158:161], v[210:213], v[230:233], v[158:161]
	s_cbranch_vccnz .LBB0_1191
	ds_read_b128 v[230:233], v3 offset:2048
	s_waitcnt lgkmcnt(0)
	v_mfma_f32_16x16x32_bf16 v[106:109], v[198:201], v[230:233], v[106:109]
	v_mfma_f32_16x16x32_bf16 v[138:141], v[202:205], v[230:233], v[138:141]
	v_mfma_f32_16x16x32_bf16 v[102:105], v[206:209], v[230:233], v[102:105]
	v_mfma_f32_16x16x32_bf16 v[110:113], v[210:213], v[230:233], v[110:113]
	v_cndmask_b32_e64 v5, 0, 1, s[58:59]
	v_cmp_ne_u32_e64 s[8:9], 1, v5
	s_andn2_b64 vcc, exec, s[58:59]
	s_cbranch_vccz .LBB0_1192

; #define LAS __attribute__((address_space(3)))
; #define G_DMA_A(buf, t, i_) __builtin_amdgcn_raw_ptr_buffer_load_lds(ra, (LAS void*)(lds + (buf) * 65536 + a_wu + (i_) * 8192), 16, ao##i_, (unsigned)(t) * 128u, 0, 0)
; #define G_DMA_A(buf, t, i_) __builtin_amdgcn_raw_ptr_buffer_load_lds(ra, (LAS void*)(lds + (buf) * 65536 + a_wu + (i_) * 8192), 16, ao##i_, (unsigned)(t) * 128u, 0, 0)
; __device__ __forceinline__ void gemm_kloop_light(f32x4 (&acc)[8][4], LAS unsigned char* lds, const GemmT& T, ...
;     ...
;     for (int t = 0; t < nt; ++t) { const int cur = t & 1; const bool w1 = t + 1 < nt, i2 = t + 2 < nt;
;         if (w1) { G_DMA_A(cur ^ 1, t + 1, 0); G_DMA_A(cur ^ 1, t + 1, 1); G_DMA_A(cur ^ 1, t + 1, 2); G_DMA_A(cur ^ 1, t + 1, 3); }
;         if (mlim > 0) {
; #pragma unroll
;             for (int ks = 0; ks < 2; ++ks) { const LAS unsigned char* s_ = lds + cur * 65536 + ks * 1024; bf16x8 Bf_[4];
; #pragma unroll
;                 for (int n_ = 0; n_ < 4; ++n_) Bf_[n_] = *(const LAS bf16x8*)(s_ + T.b_r + n_ * 2048);
; #pragma unroll
;                 for (int m_ = 0; m_ < 8; ++m_) if (m_ < mlim) { const bf16x8 At_ = *(const LAS bf16x8*)(s_ + T.a_r + m_ * 2048);
; #pragma unroll
;                     for (int n_ = 0; n_ < 4; ++n_) acc[m_][n_] = __builtin_amdgcn_mfma_f32_16x16x32_bf16(Bf_[n_], At_, acc[m_][n_], 0, 0, 0); } } }
.LBB0_1204:
	s_add_i32 m0, s3, 0x10000
	s_add_i32 s6, s3, 0x16000
	s_add_i32 s7, s3, 0x14000
	s_add_i32 s3, s3, 0x12000
	s_mov_b32 s38, s26
	s_mov_b32 s39, s27
	buffer_load_dwordx4 v223, s[36:39], s83 offen lds
	s_mov_b32 m0, s3
	v_cndmask_b32_e64 v3, 0, 1, s[60:61]
	s_cmp_lt_i32 s99, 65
	s_cbranch_scc1 .Lmy_lsk1
	buffer_load_dwordx4 v222, s[36:39], s83 offen lds
.Lmy_lsk1:
	s_mov_b32 m0, s7
	s_and_b64 vcc, exec, s[4:5]
	s_mov_b32 m0, s6
	v_cmp_ne_u32_e64 s[6:7], 1, v3
	s_cbranch_vccnz .LBB0_1221
	v_add_u32_e32 v4, 0, v226
	ds_read_b128 v[198:201], v4 offset:32768
	v_add_u32_e32 v3, 0, v216
	ds_read_b128 v[202:205], v4 offset:34816
	ds_read_b128 v[230:233], v3
	ds_read_b128 v[206:209], v4 offset:36864
	ds_read_b128 v[210:213], v4 offset:38912
	s_waitcnt lgkmcnt(2)
	v_mfma_f32_16x16x32_bf16 v[194:197], v[202:205], v[230:233], v[194:197]
	s_and_b64 vcc, exec, s[6:7]
	v_mfma_f32_16x16x32_bf16 v[154:157], v[198:201], v[230:233], v[154:157]
	s_waitcnt lgkmcnt(1)
	v_mfma_f32_16x16x32_bf16 v[150:153], v[206:209], v[230:233], v[150:153]
	s_waitcnt lgkmcnt(0)
	v_mfma_f32_16x16x32_bf16 v[158:161], v[210:213], v[230:233], v[158:161]
	s_cbranch_vccnz .LBB0_1239
	ds_read_b128 v[230:233], v3 offset:2048
	s_waitcnt lgkmcnt(0)
	v_mfma_f32_16x16x32_bf16 v[106:109], v[198:201], v[230:233], v[106:109]
	v_mfma_f32_16x16x32_bf16 v[138:141], v[202:205], v[230:233], v[138:141]
	v_mfma_f32_16x16x32_bf16 v[102:105], v[206:209], v[230:233], v[102:105]
	v_mfma_f32_16x16x32_bf16 v[110:113], v[210:213], v[230:233], v[110:113]
	v_cndmask_b32_e64 v5, 0, 1, s[58:59]
	v_cmp_ne_u32_e64 s[8:9], 1, v5
	s_andn2_b64 vcc, exec, s[58:59]
	s_cbranch_vccz .LBB0_1240

; __device__ __forceinline__ int tid_opaque() { int t = threadIdx.x; asm volatile("" : "+v"(t)); return t; }
;     __device__ __forceinline__ void init() {
;         const int tid = tid_opaque(), wid = tid >> 6, lane = tid & 63;
;         wr = wid >> 2; wc = wid & 3; fr = lane & 15; fq = lane >> 4;
;         aR = (wid >> 1) * 16 + (lane >> 2); aC = (wid & 1) * 32 + (((lane & 3) ^ ((lane >> 5) << 1)) * 8);
;         a_w = (unsigned)(wid * 1024 + lane * 16);
;         { const int l32 = lane & 31, kc8 = 2 * (wid >> 1) + (lane >> 5), wc_ = l32 >> 3, bfq = (l32 >> 1) & 3, nlo = l32 & 1; b_p = wid & 1;
;           b_k = kc8 * 8; b_col = wc_ * 64 + b_p * 32 + bfq * 8 + nlo * 4; b_gucol = wc_ * 32 + bfq * 8 + nlo * 4;
;           const int sub = wc_ * 4 + 2 * b_p + nlo;
;           b_w = (unsigned)((sub * 2 + (kc8 >> 2)) * 1024 + (((4 * bfq) * 64 + (kc8 & 3) * 16) ^ ((bfq >> 1) << 5))); b_rot = (unsigned)(nlo * 64); }
;         const unsigned lo = (unsigned)((fr * 64 + fq * 16) ^ ((fr >> 3) << 5));
;         a_r = (unsigned)(wr * 16384) + lo; b_r = 32768u + (unsigned)(wc * 8192) + lo;
; __device__ __forceinline__ void phase_moe_down(const Ptrs& p, LAS unsigned char* lds) {
;     ...
;         GemmT T; T.init();
;         const int* list = (const int*)(p.ws + OFF_LIST) + (size_t)mu.e * NTOK; const int i0 = mu.mt * 256, col0 = mu.nt * 256;
;         const unsigned ao = (unsigned)((T.aR * D + T.aC) * 2), bo = (unsigned)((T.b_k * D + T.b_col) * 4);
;         int pa = -1; float pg = 0.f;
;         { const int t_ = tid_opaque(); if (t_ < 256 && i0 + t_ < mu.cnt) { pa = list[i0 + t_]; pg = gate[pa]; } }
.LBB0_1483:
	s_or_b64 exec, exec, s[0:1]
	s_add_i32 s2, s84, s85
	s_ashr_i32 s3, s2, 31
	s_lshl_b32 s0, s81, 8
	s_lshl_b64 s[2:3], s[2:3], 12
	s_add_u32 s36, s20, s2
	v_readlane_b32 s4, v246, 0
	s_addc_u32 s1, s28, s3
	v_readlane_b32 s5, v246, 1
	v_readlane_b32 s6, v246, 2
	v_readlane_b32 s7, v246, 3
	v_readlane_b32 s8, v246, 4
	v_readlane_b32 s9, v246, 5
	s_and_b32 s37, s1, 0xffff
	s_lshl_b64 s[2:3], s[42:43], 24
	v_readlane_b32 s10, v246, 6
	v_readlane_b32 s11, v246, 7
	s_mov_b64 s[4:5], s[8:9]
	s_add_u32 s4, s4, s2
	v_ashrrev_i32_e32 v4, 6, v3
	v_bfe_u32 v11, v3, 1, 2
	s_addc_u32 s5, s5, s3
	s_ashr_i32 s1, s0, 31
	v_ashrrev_i32_e32 v5, 7, v3
	v_and_b32_e32 v6, 1, v4
	v_bfe_u32 v8, v3, 5, 1
	v_bfe_u32 v10, v3, 3, 2
	v_and_b32_e32 v12, 1, v3
	v_lshlrev_b32_e32 v14, 3, v11
	s_lshl_b64 s[2:3], s[0:1], 2
	v_lshlrev_b32_e32 v7, 5, v6
	v_lshl_or_b32 v9, v5, 1, v8
	v_lshl_or_b32 v14, v10, 6, v14
	v_lshlrev_b32_e32 v15, 2, v12
	s_add_u32 s24, s4, s2
	v_lshlrev_b32_e32 v13, 16, v9
	v_or3_b32 v14, v14, v15, v7
	s_addc_u32 s1, s5, s3
	v_lshl_or_b32 v222, v14, 2, v13
	s_and_b32 s25, s1, 0xffff
	s_movk_i32 s1, 0x2000
	buffer_load_dwordx4 v[110:113], v222, s[24:27], 0 offen
	buffer_load_dwordx4 v[114:117], v222, s[24:27], s66 offen
	s_mov_b32 s2, 0x8000
	buffer_load_dwordx4 v[122:125], v222, s[24:27], s1 offen
	buffer_load_dwordx4 v[118:121], v222, s[24:27], s2 offen
	s_movk_i32 s1, 0x4000
	s_mov_b32 s2, 0xa000
	buffer_load_dwordx4 v[126:129], v222, s[24:27], s1 offen
	buffer_load_dwordx4 v[130:133], v222, s[24:27], s2 offen
	s_mov_b32 s1, 0xc000
	s_mov_b32 s2, 0xe000
	buffer_load_dwordx4 v[138:141], v222, s[24:27], s1 offen
	buffer_load_dwordx4 v[142:145], v222, s[24:27], s2 offen
	s_waitcnt vmcnt(8)
	v_cmp_ne_u32_e32 vcc, -1, v214
	s_and_saveexec_b64 vcc, vcc
	v_ashrrev_i32_e32 v17, 31, v214
	v_mov_b32_e32 v16, v214
	v_lshl_add_u64 v[16:17], v[16:17], 2, s[56:57]
	global_load_dword v215, v[16:17], off
	s_or_b64 exec, exec, vcc
	v_lshlrev_b32_e32 v16, 3, v3
	v_and_b32_e32 v13, 63, v3
	v_lshlrev_b32_e32 v8, 4, v8
	v_and_b32_e32 v17, 24, v16
	v_bitop3_b32 v7, v8, v7, v17 bitop3:0xde
	v_lshlrev_b32_e32 v8, 4, v13
	v_lshl_or_b32 v230, v4, 10, v8
	v_lshlrev_b32_e32 v8, 2, v10
	v_lshlrev_b32_e32 v6, 1, v6
	v_or3_b32 v6, v8, v6, v12
	v_lshlrev_b32_e32 v8, 2, v3
	v_and_b32_e32 v10, 0xfffffc00, v8
	v_lshl_add_u32 v6, v6, 11, v10
	v_lshlrev_b32_e32 v10, 8, v11
	v_lshlrev_b32_e32 v9, 4, v9
	v_and_b32_e32 v15, 15, v3
	v_and_or_b32 v9, v9, 48, v10
	v_and_b32_e32 v10, 32, v16
	v_bitop3_b32 v220, v6, v9, v10 bitop3:0xf6
	v_lshlrev_b32_e32 v6, 6, v15
	v_and_b32_e32 v9, 48, v3
	v_and_b32_e32 v8, 32, v8
	v_or_b32_e32 v10, v6, v9
	v_bitop3_b32 v6, v6, v8, v9 bitop3:0x36
	v_lshlrev_b32_e32 v4, 13, v4
	v_ashrrev_i32_e32 v14, 8, v3
	v_and_or_b32 v227, v4, s66, v6
	v_lshlrev_b32_e32 v4, 16, v5
	v_lshlrev_b32_e32 v3, 10, v3
	s_mov_b32 s1, 0xf000
	v_lshlrev_b32_e32 v219, 6, v12
	v_and_or_b32 v3, v3, s1, v4
	v_lshlrev_b32_e32 v9, 14, v14
	v_lshl_or_b32 v225, v7, 1, v3
	v_cmp_eq_u32_e32 vcc, 0, v216
	v_add_u32_e32 v228, 0, v220
	v_add_u32_e32 v3, 0xc0, v219
	v_bitop3_b32 v217, v10, v9, v8 bitop3:0xde
	v_or_b32_e32 v218, 0x8000, v227
	v_readfirstlane_b32 s1, v14
	v_add_u32_e32 v226, 0x40000, v225
	v_add_u32_e32 v224, 0x80000, v225
	v_add_u32_e32 v223, 0xc0000, v225
	v_add_u32_e32 v229, v228, v219
	v_and_b32_e32 v221, 0xc0, v3
	s_mov_b64 s[6:7], s[10:11]
	s_cbranch_vccnz .LBB0_1574
; #define G_DMA_A(buf, t, i_) __builtin_amdgcn_raw_ptr_buffer_load_lds(ra, (LAS void*)(lds + (buf) * 65536 + a_wu + (i_) * 8192), 16, ao##i_, (unsigned)(t) * 128u, 0, 0)
; #define G_ISSUE_B(t) do { const unsigned so_ = (unsigned)(t) * 64u * ldbB; _Pragma("unroll") for (int i_ = 0; i_ < 8; ++i_) sb[i_] = __builtin_bit_cast(f32x4, __builtin_amdgcn_raw_buffer_load_b128(rb, bo, so_ + (unsigned)i_ * ldbB, 0)); } while (0)
; #define G_RETIRE() asm volatile("s_waitcnt vmcnt(0)" : "+v"(sb[0]), "+v"(sb[1]), "+v"(sb[2]), "+v"(sb[3]), "+v"(sb[4]), "+v"(sb[5]), "+v"(sb[6]), "+v"(sb[7]) :: "memory")
; #define G_WRITE_B(buf) do { LAS unsigned char* d_ = lds + (buf) * 65536; \
;         _Pragma("unroll") for (int j_ = 0; j_ < 4; ++j_) { u32x4 w_; w_.x = cvtpk(sb[0][j_], sb[1][j_]); w_.y = cvtpk(sb[2][j_], sb[3][j_]); w_.z = cvtpk(sb[4][j_], sb[5][j_]); w_.w = cvtpk(sb[6][j_], sb[7][j_]); \
;             *(LAS u32x4*)(d_ + 32768 + T.b_w + ((T.b_rot + 64u * j_) & 255u)) = w_; } } while (0)
; #define G_BAR() do { asm volatile("s_waitcnt lgkmcnt(0)" ::: "memory"); __builtin_amdgcn_s_barrier(); asm volatile("" ::: "memory"); } while (0)
; #define G_DMA_A(buf, t, i_) __builtin_amdgcn_raw_ptr_buffer_load_lds(ra, (LAS void*)(lds + (buf) * 65536 + a_wu + (i_) * 8192), 16, ao##i_, (unsigned)(t) * 128u, 0, 0)
; #define G_ISSUE_B(t) do { const unsigned so_ = (unsigned)(t) * 64u * ldbB; _Pragma("unroll") for (int i_ = 0; i_ < 8; ++i_) sb[i_] = __builtin_bit_cast(f32x4, __builtin_amdgcn_raw_buffer_load_b128(rb, bo, so_ + (unsigned)i_ * ldbB, 0)); } while (0)
; #define G_RETIRE() asm volatile("s_waitcnt vmcnt(0)" : "+v"(sb[0]), "+v"(sb[1]), "+v"(sb[2]), "+v"(sb[3]), "+v"(sb[4]), "+v"(sb[5]), "+v"(sb[6]), "+v"(sb[7]) :: "memory")
; __device__ __forceinline__ void gemm_kloop_light(f32x4 (&acc)[8][4], LAS unsigned char* lds, const GemmT& T, ...
;     ...
;     G_ISSUE_B(0); G_DMA_A(0, 0, 0); G_DMA_A(0, 0, 1); G_DMA_A(0, 0, 2); G_DMA_A(0, 0, 3); G_RETIRE(); G_WRITE_B(0);
;     if (nt > 1) G_ISSUE_B(1);
;     G_BAR();
; __device__ __forceinline__ void phase_moe_down(const Ptrs& p, LAS unsigned char* lds) {
;     ...
;         const int mlim = __builtin_amdgcn_readfirstlane(T.wr) ? 0 : ((mu.cnt - i0 + 15) >> 4);
	s_sub_i32 s2, s83, s85
	s_mov_b32 s99, s2
	s_add_i32 s2, s2, 15
	s_ashr_i32 s2, s2, 4
	s_cmp_eq_u32 s1, 0
	s_cselect_b32 s1, s2, 0
	v_readfirstlane_b32 s2, v230
	s_and_b32 s2, s2, 0xfffffc00
	s_add_i32 s2, s2, 0
	s_mov_b32 s38, s26
	s_mov_b32 s39, s27
	s_mov_b32 m0, s2
	s_waitcnt vmcnt(4)
	v_mov_b64_e32 v[4:5], v[118:119]
	buffer_load_dwordx4 v225, s[36:39], 0 offen lds
	s_add_i32 m0, s2, 0x2000
	s_waitcnt vmcnt(2)
	v_mov_b64_e32 v[8:9], v[138:139]
	buffer_load_dwordx4 v226, s[36:39], 0 offen lds
	s_add_i32 m0, s2, 0x4000
	v_mov_b64_e32 v[12:13], v[122:123]
	buffer_load_dwordx4 v224, s[36:39], 0 offen lds
	s_add_i32 m0, s2, 0x6000
	v_mov_b64_e32 v[16:17], v[114:115]
	v_mov_b64_e32 v[20:21], v[130:131]
	v_mov_b64_e32 v[24:25], v[110:111]
	s_waitcnt vmcnt(3)
	v_mov_b64_e32 v[28:29], v[142:143]
	v_mov_b64_e32 v[32:33], v[126:127]
	buffer_load_dwordx4 v223, s[36:39], 0 offen lds
	v_mov_b64_e32 v[6:7], v[120:121]
	v_mov_b64_e32 v[10:11], v[140:141]
	v_mov_b64_e32 v[14:15], v[124:125]
	v_mov_b64_e32 v[18:19], v[116:117]
	v_mov_b64_e32 v[22:23], v[132:133]
	v_mov_b64_e32 v[26:27], v[112:113]
	v_mov_b64_e32 v[30:31], v[144:145]
	v_mov_b64_e32 v[34:35], v[128:129]
	s_waitcnt vmcnt(0)
	buffer_load_dwordx4 v[162:165], v222, s[24:27], s67 offen
	buffer_load_dwordx4 v[170:173], v222, s[24:27], s68 offen
	buffer_load_dwordx4 v[174:177], v222, s[24:27], s69 offen
	buffer_load_dwordx4 v[178:181], v222, s[24:27], s70 offen
	buffer_load_dwordx4 v[182:185], v222, s[24:27], s71 offen
	buffer_load_dwordx4 v[186:189], v222, s[24:27], s76 offen
	buffer_load_dwordx4 v[190:193], v222, s[24:27], s77 offen
	buffer_load_dwordx4 v[194:197], v222, s[24:27], s78 offen
	s_cmp_gt_i32 s1, 0
	s_cselect_b64 s[60:61], -1, 0
	s_cmp_lg_u32 s1, 1
	v_cvt_pk_bf16_f32 v36, v24, v12
	v_cvt_pk_bf16_f32 v37, v32, v16
	v_cvt_pk_bf16_f32 v38, v4, v20
	v_cvt_pk_bf16_f32 v39, v8, v28
	s_cselect_b64 s[58:59], -1, 0
	s_cmp_gt_i32 s1, 2
	ds_write_b128 v229, v[36:39] offset:32768
	v_cvt_pk_bf16_f32 v36, v25, v13
	v_cvt_pk_bf16_f32 v37, v33, v17
	v_cvt_pk_bf16_f32 v38, v5, v21
	v_cvt_pk_bf16_f32 v39, v9, v29
	s_cselect_b64 s[54:55], -1, 0
	s_cmp_gt_i32 s1, 3
	ds_write_b128 v229, v[36:39] offset:32832
	v_cvt_pk_bf16_f32 v36, v26, v14
	v_cvt_pk_bf16_f32 v37, v34, v18
	v_cvt_pk_bf16_f32 v38, v6, v22
	v_cvt_pk_bf16_f32 v39, v10, v30
	v_cvt_pk_bf16_f32 v4, v27, v15
	v_cvt_pk_bf16_f32 v5, v35, v19
	v_cvt_pk_bf16_f32 v6, v7, v23
	v_cvt_pk_bf16_f32 v7, v11, v31
	v_add_u32_e32 v3, v228, v221
	s_cselect_b64 s[50:51], -1, 0
	s_cmp_gt_i32 s1, 4
	ds_write_b128 v229, v[36:39] offset:32896
	ds_write_b128 v3, v[4:7] offset:32768
	s_cselect_b64 s[48:49], -1, 0
	s_cmp_gt_i32 s1, 5
	s_waitcnt lgkmcnt(0)
	s_barrier
	s_cselect_b64 s[46:47], -1, 0
	s_cmp_gt_i32 s1, 6
	v_mov_b32_e32 v4, v2
	v_mov_b32_e32 v5, v2
	s_cselect_b64 s[44:45], -1, 0
	s_cmp_gt_i32 s1, 7
	v_mov_b32_e32 v3, v2
	v_mov_b64_e32 v[12:13], v[4:5]
	v_mov_b64_e32 v[8:9], v[4:5]
	v_mov_b64_e32 v[20:21], v[4:5]
	v_mov_b64_e32 v[16:17], v[4:5]
	v_mov_b64_e32 v[28:29], v[4:5]
	v_mov_b64_e32 v[24:25], v[4:5]
	v_mov_b64_e32 v[36:37], v[4:5]
	v_mov_b64_e32 v[32:33], v[4:5]
	v_mov_b64_e32 v[44:45], v[4:5]
	v_mov_b64_e32 v[40:41], v[4:5]
	v_mov_b64_e32 v[52:53], v[4:5]
	v_mov_b64_e32 v[48:49], v[4:5]
	v_mov_b64_e32 v[60:61], v[4:5]
	v_mov_b64_e32 v[56:57], v[4:5]
	v_mov_b64_e32 v[68:69], v[4:5]
	v_mov_b64_e32 v[64:65], v[4:5]
	v_mov_b64_e32 v[76:77], v[4:5]
	v_mov_b64_e32 v[72:73], v[4:5]
	v_mov_b64_e32 v[84:85], v[4:5]
	v_mov_b64_e32 v[80:81], v[4:5]
	v_mov_b64_e32 v[92:93], v[4:5]
	v_mov_b64_e32 v[88:89], v[4:5]
	v_mov_b64_e32 v[100:101], v[4:5]
	v_mov_b64_e32 v[96:97], v[4:5]
	v_mov_b64_e32 v[108:109], v[4:5]
	v_mov_b64_e32 v[104:105], v[4:5]
	v_mov_b64_e32 v[148:149], v[4:5]
	v_mov_b64_e32 v[136:137], v[4:5]
	v_mov_b64_e32 v[156:157], v[4:5]
	v_mov_b64_e32 v[152:153], v[4:5]
	v_mov_b64_e32 v[168:169], v[4:5]
	v_mov_b64_e32 v[160:161], v[4:5]
	s_mov_b32 s3, 0
	s_cselect_b64 s[34:35], -1, 0
	s_mov_b32 s72, 0x10e000
	s_movk_i32 s73, 0x80
	v_mov_b64_e32 v[10:11], v[2:3]
	v_mov_b64_e32 v[6:7], v[2:3]
	v_mov_b64_e32 v[18:19], v[2:3]
	v_mov_b64_e32 v[14:15], v[2:3]
	v_mov_b64_e32 v[26:27], v[2:3]
	v_mov_b64_e32 v[22:23], v[2:3]
	v_mov_b64_e32 v[34:35], v[2:3]
	v_mov_b64_e32 v[30:31], v[2:3]
	v_mov_b64_e32 v[42:43], v[2:3]
	v_mov_b64_e32 v[38:39], v[2:3]
	v_mov_b64_e32 v[50:51], v[2:3]
	v_mov_b64_e32 v[46:47], v[2:3]
	v_mov_b64_e32 v[58:59], v[2:3]
	v_mov_b64_e32 v[54:55], v[2:3]
	v_mov_b64_e32 v[66:67], v[2:3]
	v_mov_b64_e32 v[62:63], v[2:3]
	v_mov_b64_e32 v[74:75], v[2:3]
	v_mov_b64_e32 v[70:71], v[2:3]
	v_mov_b64_e32 v[82:83], v[2:3]
	v_mov_b64_e32 v[78:79], v[2:3]
	v_mov_b64_e32 v[90:91], v[2:3]
	v_mov_b64_e32 v[86:87], v[2:3]
	v_mov_b64_e32 v[98:99], v[2:3]
	v_mov_b64_e32 v[94:95], v[2:3]
	v_mov_b64_e32 v[106:107], v[2:3]
	v_mov_b64_e32 v[102:103], v[2:3]
	v_mov_b64_e32 v[146:147], v[2:3]
	v_mov_b64_e32 v[134:135], v[2:3]
	v_mov_b64_e32 v[154:155], v[2:3]
	v_mov_b64_e32 v[150:151], v[2:3]
	v_mov_b64_e32 v[166:167], v[2:3]
	v_mov_b64_e32 v[158:159], v[2:3]
	s_branch .LBB0_1486

; #define LAS __attribute__((address_space(3)))
; #define G_DMA_A(buf, t, i_) __builtin_amdgcn_raw_ptr_buffer_load_lds(ra, (LAS void*)(lds + (buf) * 65536 + a_wu + (i_) * 8192), 16, ao##i_, (unsigned)(t) * 128u, 0, 0)
; #define G_DMA_A(buf, t, i_) __builtin_amdgcn_raw_ptr_buffer_load_lds(ra, (LAS void*)(lds + (buf) * 65536 + a_wu + (i_) * 8192), 16, ao##i_, (unsigned)(t) * 128u, 0, 0)
; __device__ __forceinline__ void gemm_kloop_light(f32x4 (&acc)[8][4], LAS unsigned char* lds, const GemmT& T, ...
;     ...
;     for (int t = 0; t < nt; ++t) { const int cur = t & 1; const bool w1 = t + 1 < nt, i2 = t + 2 < nt;
;         if (w1) { G_DMA_A(cur ^ 1, t + 1, 0); G_DMA_A(cur ^ 1, t + 1, 1); G_DMA_A(cur ^ 1, t + 1, 2); G_DMA_A(cur ^ 1, t + 1, 3); }
;         if (mlim > 0) {
; #pragma unroll
;             for (int ks = 0; ks < 2; ++ks) { const LAS unsigned char* s_ = lds + cur * 65536 + ks * 1024; bf16x8 Bf_[4];
; #pragma unroll
;                 for (int n_ = 0; n_ < 4; ++n_) Bf_[n_] = *(const LAS bf16x8*)(s_ + T.b_r + n_ * 2048);
; #pragma unroll
;                 for (int m_ = 0; m_ < 8; ++m_) if (m_ < mlim) { const bf16x8 At_ = *(const LAS bf16x8*)(s_ + T.a_r + m_ * 2048);
; #pragma unroll
;                     for (int n_ = 0; n_ < 4; ++n_) acc[m_][n_] = __builtin_amdgcn_mfma_f32_16x16x32_bf16(Bf_[n_], At_, acc[m_][n_], 0, 0, 0); } } }
.LBB0_1486:
	s_and_b32 s6, s3, 0x10000
	s_xor_b32 s74, s6, 0x10000
	s_add_i32 s4, s2, s74
	s_mov_b32 m0, s4
	s_add_i32 s5, s4, 0x6000
	s_add_i32 s7, s4, 0x4000
	s_addk_i32 s4, 0x2000
	buffer_load_dwordx4 v225, s[36:39], s73 offen lds
	s_mov_b32 m0, s4
	v_cndmask_b32_e64 v3, 0, 1, s[60:61]
	s_cmp_lt_i32 s99, 65
	s_cbranch_scc1 .Lmy_lsk2
	buffer_load_dwordx4 v226, s[36:39], s73 offen lds
.Lmy_lsk2:
	s_mov_b32 m0, s7
	s_andn2_b64 vcc, exec, s[60:61]
	s_mov_b32 m0, s5
	v_cmp_ne_u32_e64 s[4:5], 1, v3
	s_cbranch_vccnz .LBB0_1485
	s_add_i32 s6, s6, 0
	v_add_u32_e32 v4, s6, v227
	ds_read_b128 v[198:201], v4 offset:32768
	v_add_u32_e32 v3, s6, v217
	ds_read_b128 v[202:205], v4 offset:34816
	ds_read_b128 v[232:235], v3
	ds_read_b128 v[206:209], v4 offset:36864
	ds_read_b128 v[210:213], v4 offset:38912
	s_waitcnt lgkmcnt(2)
	v_mfma_f32_16x16x32_bf16 v[166:169], v[202:205], v[232:235], v[166:169]
	v_cndmask_b32_e64 v5, 0, 1, s[58:59]
	v_cmp_ne_u32_e64 s[6:7], 1, v5
	s_andn2_b64 vcc, exec, s[58:59]
	v_mfma_f32_16x16x32_bf16 v[158:161], v[198:201], v[232:235], v[158:161]
	s_waitcnt lgkmcnt(1)
	v_mfma_f32_16x16x32_bf16 v[150:153], v[206:209], v[232:235], v[150:153]
	s_waitcnt lgkmcnt(0)
	v_mfma_f32_16x16x32_bf16 v[154:157], v[210:213], v[232:235], v[154:157]
	s_cbranch_vccnz .LBB0_1502
	ds_read_b128 v[232:235], v3 offset:2048
	s_waitcnt lgkmcnt(0)
	v_mfma_f32_16x16x32_bf16 v[134:137], v[198:201], v[232:235], v[134:137]
	v_mfma_f32_16x16x32_bf16 v[146:149], v[202:205], v[232:235], v[146:149]
	v_mfma_f32_16x16x32_bf16 v[102:105], v[206:209], v[232:235], v[102:105]
	v_mfma_f32_16x16x32_bf16 v[106:109], v[210:213], v[232:235], v[106:109]
	v_cndmask_b32_e64 v5, 0, 1, s[54:55]
	v_cmp_ne_u32_e64 s[8:9], 1, v5
	s_andn2_b64 vcc, exec, s[54:55]
	s_cbranch_vccz .LBB0_1503

; #define LAS __attribute__((address_space(3)))
; #define G_DMA_A(buf, t, i_) __builtin_amdgcn_raw_ptr_buffer_load_lds(ra, (LAS void*)(lds + (buf) * 65536 + a_wu + (i_) * 8192), 16, ao##i_, (unsigned)(t) * 128u, 0, 0)
; #define G_DMA_A(buf, t, i_) __builtin_amdgcn_raw_ptr_buffer_load_lds(ra, (LAS void*)(lds + (buf) * 65536 + a_wu + (i_) * 8192), 16, ao##i_, (unsigned)(t) * 128u, 0, 0)
; __device__ __forceinline__ void gemm_kloop_light(f32x4 (&acc)[8][4], LAS unsigned char* lds, const GemmT& T, ...
;     ...
;     for (int t = 0; t < nt; ++t) { const int cur = t & 1; const bool w1 = t + 1 < nt, i2 = t + 2 < nt;
;         if (w1) { G_DMA_A(cur ^ 1, t + 1, 0); G_DMA_A(cur ^ 1, t + 1, 1); G_DMA_A(cur ^ 1, t + 1, 2); G_DMA_A(cur ^ 1, t + 1, 3); }
;         if (mlim > 0) {
; #pragma unroll
;             for (int ks = 0; ks < 2; ++ks) { const LAS unsigned char* s_ = lds + cur * 65536 + ks * 1024; bf16x8 Bf_[4];
; #pragma unroll
;                 for (int n_ = 0; n_ < 4; ++n_) Bf_[n_] = *(const LAS bf16x8*)(s_ + T.b_r + n_ * 2048);
; #pragma unroll
;                 for (int m_ = 0; m_ < 8; ++m_) if (m_ < mlim) { const bf16x8 At_ = *(const LAS bf16x8*)(s_ + T.a_r + m_ * 2048);
; #pragma unroll
;                     for (int n_ = 0; n_ < 4; ++n_) acc[m_][n_] = __builtin_amdgcn_mfma_f32_16x16x32_bf16(Bf_[n_], At_, acc[m_][n_], 0, 0, 0); } } }
.LBB0_1515:
	s_add_i32 m0, s2, 0x10000
	s_add_i32 s3, s2, 0x16000
	s_add_i32 s6, s2, 0x14000
	s_add_i32 s2, s2, 0x12000
	s_mov_b32 s38, s26
	s_mov_b32 s39, s27
	buffer_load_dwordx4 v225, s[36:39], s79 offen lds
	s_mov_b32 m0, s2
	v_cndmask_b32_e64 v3, 0, 1, s[58:59]
	s_cmp_lt_i32 s99, 65
	s_cbranch_scc1 .Lmy_lsk3
	buffer_load_dwordx4 v226, s[36:39], s79 offen lds
.Lmy_lsk3:
	s_mov_b32 m0, s6
	s_and_b64 vcc, exec, s[4:5]
	s_mov_b32 m0, s3
	v_cmp_ne_u32_e64 s[6:7], 1, v3
	s_cbranch_vccnz .LBB0_1532
	v_add_u32_e32 v4, 0, v227
	ds_read_b128 v[198:201], v4 offset:32768
	v_add_u32_e32 v3, 0, v217
	ds_read_b128 v[202:205], v4 offset:34816
	ds_read_b128 v[232:235], v3
	ds_read_b128 v[206:209], v4 offset:36864
	ds_read_b128 v[210:213], v4 offset:38912
	s_waitcnt lgkmcnt(2)
	v_mfma_f32_16x16x32_bf16 v[166:169], v[202:205], v[232:235], v[166:169]
	s_and_b64 vcc, exec, s[6:7]
	v_mfma_f32_16x16x32_bf16 v[158:161], v[198:201], v[232:235], v[158:161]
	s_waitcnt lgkmcnt(1)
	v_mfma_f32_16x16x32_bf16 v[150:153], v[206:209], v[232:235], v[150:153]
	s_waitcnt lgkmcnt(0)
	v_mfma_f32_16x16x32_bf16 v[154:157], v[210:213], v[232:235], v[154:157]
	s_cbranch_vccnz .LBB0_1550
	ds_read_b128 v[232:235], v3 offset:2048
	s_waitcnt lgkmcnt(0)
	v_mfma_f32_16x16x32_bf16 v[134:137], v[198:201], v[232:235], v[134:137]
	v_mfma_f32_16x16x32_bf16 v[146:149], v[202:205], v[232:235], v[146:149]
	v_mfma_f32_16x16x32_bf16 v[102:105], v[206:209], v[232:235], v[102:105]
	v_mfma_f32_16x16x32_bf16 v[106:109], v[210:213], v[232:235], v[106:109]
	v_cndmask_b32_e64 v5, 0, 1, s[54:55]
	v_cmp_ne_u32_e64 s[8:9], 1, v5
	s_andn2_b64 vcc, exec, s[54:55]
	s_cbranch_vccz .LBB0_1551

; __global__ void __launch_bounds__(512, 2) mega_fwd(Ptrs p) {
	.amdhsa_kernel _Z8mega_fwd4Ptrs
		.amdhsa_group_segment_fixed_size 0
		.amdhsa_private_segment_fixed_size 0
		.amdhsa_kernarg_size 440
		.amdhsa_user_sgpr_count 2
		.amdhsa_user_sgpr_dispatch_ptr 0
		.amdhsa_user_sgpr_queue_ptr 0
		.amdhsa_user_sgpr_kernarg_segment_ptr 1
		.amdhsa_user_sgpr_dispatch_id 0
		.amdhsa_user_sgpr_kernarg_preload_length 0
		.amdhsa_user_sgpr_kernarg_preload_offset 0
		.amdhsa_user_sgpr_private_segment_size 0
		.amdhsa_uses_dynamic_stack 0
		.amdhsa_enable_private_segment 0
		.amdhsa_system_sgpr_workgroup_id_x 1
		.amdhsa_system_sgpr_workgroup_id_y 0
		.amdhsa_system_sgpr_workgroup_id_z 0
		.amdhsa_system_sgpr_workgroup_info 0
		.amdhsa_system_vgpr_workitem_id 0
		.amdhsa_next_free_vgpr 256
		.amdhsa_next_free_sgpr 102
		.amdhsa_accum_offset 256
		.amdhsa_reserve_vcc 1
		.amdhsa_float_round_mode_32 0
		.amdhsa_float_round_mode_16_64 0
		.amdhsa_float_denorm_mode_32 3
		.amdhsa_float_denorm_mode_16_64 3
		.amdhsa_dx10_clamp 1
		.amdhsa_ieee_mode 1
		.amdhsa_fp16_overflow 0
		.amdhsa_tg_split 0
		.amdhsa_exception_fp_ieee_invalid_op 0
		.amdhsa_exception_fp_denorm_src 0
		.amdhsa_exception_fp_ieee_div_zero 0
		.amdhsa_exception_fp_ieee_overflow 0
		.amdhsa_exception_fp_ieee_underflow 0
		.amdhsa_exception_fp_ieee_inexact 0
		.amdhsa_exception_int_div_zero 0
	.end_amdhsa_kernel

; __global__ void __launch_bounds__(512, 2) mega_fwd(Ptrs p) {
amdhsa.kernels:
  - .agpr_count:     0
    .args:
      - .offset:         0
        .size:           184
        .value_kind:     by_value
      - .offset:         184
        .size:           4
        .value_kind:     hidden_block_count_x
      - .offset:         188
        .size:           4
        .value_kind:     hidden_block_count_y
      - .offset:         192
        .size:           4
        .value_kind:     hidden_block_count_z
      - .offset:         196
        .size:           2
        .value_kind:     hidden_group_size_x
      - .offset:         198
        .size:           2
        .value_kind:     hidden_group_size_y
      - .offset:         200
        .size:           2
        .value_kind:     hidden_group_size_z
      - .offset:         202
        .size:           2
        .value_kind:     hidden_remainder_x
      - .offset:         204
        .size:           2
        .value_kind:     hidden_remainder_y
      - .offset:         206
        .size:           2
        .value_kind:     hidden_remainder_z
      - .offset:         224
        .size:           8
        .value_kind:     hidden_global_offset_x
      - .offset:         232
        .size:           8
        .value_kind:     hidden_global_offset_y
      - .offset:         240
        .size:           8
        .value_kind:     hidden_global_offset_z
      - .offset:         248
        .size:           2
        .value_kind:     hidden_grid_dims
      - .offset:         304
        .size:           4
        .value_kind:     hidden_dynamic_lds_size
    .group_segment_fixed_size: 0
    .kernarg_segment_align: 8
    .kernarg_segment_size: 440
    .language:       OpenCL C
    .language_version:
      - 2
      - 0
    .max_flat_workgroup_size: 512
    .name:           _Z8mega_fwd4Ptrs
    .private_segment_fixed_size: 0
    .sgpr_count:     108
    .sgpr_spill_count: 28
    .symbol:         _Z8mega_fwd4Ptrs.kd
    .uniform_work_group_size: 1
    .uses_dynamic_stack: false
    .vgpr_count:     256
    .vgpr_spill_count: 0
    .wavefront_size: 64
